# weight-conversion schedule: out_proj l0 spare share 800 -> 480 blocks, in_proj l1 spare 210 -> 530 (spare workgroups of out_proj l0 were its critical path)
# baseline (speedup 1.0000x reference)
.LBB0_310:
	s_lshl_b32 s4, s2, 3
	v_writelane_b32 v254, s4, 7
	s_lshl_b32 s4, s3, 3
	v_writelane_b32 v254, s4, 8
	s_lshl_b32 s4, s2, 9
	s_lshl_b32 s62, s3, 9
	s_cmp_eq_u32 s2, 0
	v_writelane_b32 v254, s4, 9
	s_cselect_b64 s[4:5], -1, 0
	v_writelane_b32 v254, s4, 10
	s_lshl_b32 s8, s2, 5
	s_and_b32 s14, s87, 31
	v_writelane_b32 v254, s5, 11
	s_mul_i32 s4, s2, 0x6b
	s_add_i32 s7, s4, 0xffffd954
	s_ashr_i32 s11, s87, 5
	s_lshl_b32 s4, s2, 4
	s_lshl_b32 s66, s3, 4
	s_cmpk_lt_i32 s2, 0x100
	v_writelane_b32 v254, s4, 12
	s_cselect_b64 s[4:5], -1, 0
	v_writelane_b32 v254, s4, 13
	s_movk_i32 s64, 0x80
	s_movk_i32 s65, 0xff00
	v_writelane_b32 v254, s5, 14
	s_lshr_b32 s4, s2, 3
	s_mul_i32 s4, s4, 5
	s_and_b32 s5, s2, 7
	s_add_i32 s4, s4, s5
	s_add_i32 s4, s4, -3
	s_cmp_lt_u32 s5, 3
	s_cselect_b32 s4, 0x7fff, s4
	s_cmpk_lt_i32 s4, 0x80
	v_writelane_b32 v254, s4, 15
	s_cselect_b64 s[4:5], -1, 0
	s_and_b32 s9, s87, 3
	v_writelane_b32 v254, s4, 16
	s_cmpk_lt_i32 s2, 0x200
	s_movk_i32 s56, 0x1000
	v_writelane_b32 v254, s5, 17
	s_cselect_b64 s[4:5], -1, 0
	v_writelane_b32 v254, s4, 18
	s_lshl_b32 s74, s3, 5
	s_movk_i32 s77, 0x4400
	v_writelane_b32 v254, s5, 19
	s_lshl_b32 s4, s2, 2
	s_and_b32 s4, s4, 0xffffff00
	v_writelane_b32 v254, s4, 20
	s_lshl_b32 s4, s2, 6
	s_and_b32 s6, s4, 0xfc0
	s_cmp_gt_i32 s3, 0
	v_writelane_b32 v254, s4, 21
	s_cselect_b64 s[4:5], -1, 0
	v_writelane_b32 v254, s4, 22
	s_ashr_i32 s12, s87, 2
	s_mov_b32 s10, s12
	v_writelane_b32 v254, s5, 23
	s_ashr_i32 s4, s87, 3
	v_writelane_b32 v254, s4, 24
	s_and_b32 s5, s87, 7
	s_lshl_b32 s4, s5, 7
	v_writelane_b32 v254, s5, 25
	s_lshl_b32 s5, s5, 18
	v_writelane_b32 v254, s5, 26
	s_ashr_i32 s13, s12, 31
	v_writelane_b32 v254, s10, 27
	s_lshl_b64 s[12:13], s[12:13], 18
	s_lshl_b32 s5, s9, 8
	v_writelane_b32 v254, s11, 28
	v_writelane_b32 v254, s12, 29
	s_mov_b32 s38, 0x78787879
	s_movk_i32 s39, 0xef00
	v_writelane_b32 v254, s13, 30
	v_writelane_b32 v254, s9, 31
	s_lshl_b32 s9, s9, 18
	s_cmpk_lt_i32 s2, 0x84
	v_writelane_b32 v254, s9, 32
	s_cselect_b32 s9, 32, 0x6b
	v_writelane_b32 v254, s9, 33
	v_writelane_b32 v254, s8, 34
	s_cselect_b32 s7, s8, s7
	v_writelane_b32 v254, s7, 35
	s_add_i32 s7, s3, -1
	s_cmp_gt_u32 s7, 6
	s_cselect_b64 s[8:9], -1, 0
	s_abs_i32 s12, s3
	v_cvt_f32_u32_e32 v1, s12
	v_writelane_b32 v254, s8, 36
	s_sub_i32 s7, 0, s12
	s_and_b32 s76, s3, 0x7ffffff8
	v_rcp_iflag_f32_e32 v1, v1
	v_writelane_b32 v254, s9, 37
	s_ashr_i32 s13, s3, 31
	s_mov_b32 s59, 0x800000
	v_mul_f32_e32 v1, 0x4f7ffffe, v1
	v_cvt_u32_f32_e32 v1, v1
	v_mov_b32_e32 v205, 1
	v_mov_b32_e32 v221, 0x1400
	v_mov_b32_e32 v204, 0x20200
	v_readfirstlane_b32 s8, v1
	s_mul_i32 s7, s7, s8
	s_mul_hi_u32 s7, s8, s7
	s_add_i32 s7, s8, s7
	v_writelane_b32 v254, s7, 38
	s_mul_hi_u32 s7, s7, 0x9e9
	s_mul_i32 s8, s7, s12
	s_sub_i32 s8, 0x9e9, s8
	s_add_i32 s9, s7, 1
	s_sub_i32 s10, s8, s12
	s_cmp_ge_u32 s8, s12
	s_cselect_b32 s7, s9, s7
	s_cselect_b32 s8, s10, s8
	s_add_i32 s9, s7, 1
	s_cmp_ge_u32 s8, s12
	s_cselect_b32 s7, s9, s7
	s_xor_b32 s7, s7, s13
	s_sub_i32 s7, s7, s13
	s_mul_i32 s8, s7, s3
	s_sub_i32 s8, 0x9e9, s8
	s_mul_i32 s9, s7, s87
	s_min_i32 s10, s87, s8
	v_writelane_b32 v254, s12, 39
	s_add_i32 s9, s9, s10
	v_writelane_b32 v254, s13, 40
	s_cmp_lt_i32 s87, s8
	v_writelane_b32 v254, s9, 41
	s_cselect_b64 s[8:9], -1, 0
	s_cmp_lg_u64 s[8:9], 0
	s_addc_u32 s7, s7, 0
	v_writelane_b32 v254, s7, 42
	s_lshl_b32 s7, s3, 1
	v_writelane_b32 v254, s7, 43
	s_add_i32 s7, s11, 17
	v_writelane_b32 v254, s7, 44
	s_lshl_b32 s7, s7, 4
	v_writelane_b32 v254, s7, 45
	s_lshl_b32 s7, s14, 4
	v_writelane_b32 v254, s14, 46
	s_add_i32 s8, s7, 0xbe50
	v_writelane_b32 v254, s8, 47
	s_add_i32 s8, s11, 9
	v_writelane_b32 v254, s8, 48
	s_lshl_b32 s8, s8, 4
	v_writelane_b32 v254, s8, 49
	v_writelane_b32 v254, s11, 50
	s_add_i32 s8, s11, 1
	v_writelane_b32 v254, s8, 51
	s_or_b32 s8, s7, 0xfffffe00
	v_writelane_b32 v254, s8, 52
	s_lshl_b32 s8, s3, 6
	v_writelane_b32 v254, s8, 53
	s_add_i32 s7, s7, 0xa050
	v_writelane_b32 v254, s7, 54
	s_add_i32 s7, 0, 0x12000
	v_writelane_b32 v254, s7, 55
	s_add_i32 s7, 0, 0x27020
	v_writelane_b32 v254, s7, 56
	s_add_i32 s7, 0, 0x27024
	v_writelane_b32 v254, s7, 57
	s_add_i32 s7, 0, 0x25000
	v_writelane_b32 v254, s7, 58
	s_lshl_b32 s6, s6, 1
	v_writelane_b32 v254, s6, 59
	s_lshl_b32 s5, s5, 2
	v_writelane_b32 v254, s5, 60
	s_add_i32 s5, 0, 0x25400
	v_writelane_b32 v254, s5, 61
	s_add_i32 s5, 0, 0x10200
	v_writelane_b32 v254, s5, 62
	s_add_i32 s5, 0, 0x20100
	v_writelane_b32 v254, s5, 63
	s_add_i32 s5, 0, 0x20010
	v_writelane_b32 v255, s5, 0
	s_add_i32 s5, 0, 0x20110
	v_writelane_b32 v255, s5, 1
	s_add_i32 s5, 0, 0x20020
	v_writelane_b32 v255, s5, 2
	s_add_i32 s5, 0, 0x20120
	v_writelane_b32 v255, s5, 3
	s_add_i32 s5, 0, 0x20030
	v_writelane_b32 v255, s5, 4
	s_add_i32 s5, 0, 0x20130
	v_writelane_b32 v255, s5, 5
	s_add_i32 s5, 0, 0x20040
	v_writelane_b32 v255, s5, 6
	s_add_i32 s5, 0, 0x20140
	v_writelane_b32 v255, s5, 7
	s_add_i32 s5, 0, 0x20050
	v_writelane_b32 v255, s5, 8
	s_add_i32 s5, 0, 0x20150
	v_writelane_b32 v255, s5, 9
	s_add_i32 s5, 0, 0x20060
	v_writelane_b32 v255, s5, 10
	s_add_i32 s5, 0, 0x20160
	v_writelane_b32 v255, s5, 11
	s_add_i32 s5, 0, 0x20070
	v_writelane_b32 v255, s5, 12
	s_add_i32 s5, 0, 0x20170
	v_writelane_b32 v255, s5, 13
	s_add_i32 s5, 0, 0x20180
	v_writelane_b32 v255, s5, 14
	s_add_i32 s5, 0, 0x20084
	v_writelane_b32 v255, s5, 15
	s_add_i32 s5, 0, 0x20024
	v_writelane_b32 v255, s5, 16
	s_add_i32 s5, 0, 0x2002c
	v_writelane_b32 v255, s5, 17
	s_add_i32 s5, 0, 0x20034
	v_writelane_b32 v255, s5, 18
	s_add_i32 s5, 0, 0x2003c
	v_writelane_b32 v255, s5, 19
	s_add_i32 s5, 0, 0x20044
	v_writelane_b32 v255, s5, 20
	s_add_i32 s5, 0, 0x2004c
	v_writelane_b32 v255, s5, 21
	s_add_i32 s5, 0, 0x20054
	v_writelane_b32 v255, s5, 22
	s_add_i32 s5, 0, 0x2005c
	v_writelane_b32 v255, s5, 23
	s_add_i32 s5, 0, 0x20064
	v_writelane_b32 v255, s5, 24
	s_add_i32 s5, 0, 0x2006c
	v_writelane_b32 v255, s5, 25
	s_add_i32 s5, 0, 0x20074
	v_writelane_b32 v255, s5, 26
	s_add_i32 s5, 0, 0x2007c
	v_writelane_b32 v255, s5, 27
	s_add_i32 s5, 0, 0x20800
	v_writelane_b32 v255, s5, 28
	s_lshl_b32 s4, s4, 2
	v_writelane_b32 v255, s4, 29
	s_ashr_i32 s63, s62, 31
	s_ashr_i32 s67, s66, 31
	v_writelane_b32 v255, s5, 30
	v_cmp_eq_u32_e64 s[4:5], 0, v0
	s_mov_b32 s6, s74
	s_add_i32 s84, 0, 0x20004
	v_writelane_b32 v255, s4, 31
	s_add_i32 s69, 0, 0x2000c
	s_add_i32 s68, 0, 0x20014
	v_writelane_b32 v255, s5, 32
	s_lshl_b64 s[4:5], s[62:63], 2
	v_writelane_b32 v255, s4, 33
	s_add_i32 s49, 0, 0x2001c
	v_mov_b32_e32 v1, 0
	v_writelane_b32 v255, s5, 34
	s_lshl_b64 s[4:5], s[66:67], 12
	v_writelane_b32 v255, s4, 35
	v_mov_b32_e32 v220, 0xff800000
	s_movk_i32 s47, 0x3ff
	v_writelane_b32 v255, s5, 36
	v_writelane_b32 v255, s6, 37
	s_mov_b32 s83, 0x34400000
	s_mov_b32 s80, 0x36500000
	v_writelane_b32 v255, s7, 38
	s_mov_b32 s6, s62
	v_writelane_b32 v255, s6, 39
	s_movk_i32 s81, 0x7fff
	s_mov_b32 s57, 0x41000000
	v_writelane_b32 v255, s7, 40
	s_mov_b32 s6, s66
	v_writelane_b32 v255, s6, 41
	s_movk_i32 s33, 0xfefe
	s_mov_b32 s85, 0x900000
	v_writelane_b32 v255, s7, 42
	v_writelane_b32 v255, s76, 43
	v_writelane_b32 v255, s84, 44
	s_mov_b32 s72, 0xc0e00000
	s_mov_b32 s73, 0
	s_mov_b32 s71, 0
	s_mov_b64 s[4:5], -1
	s_mov_b64 s[78:79], 0x80
	s_mov_b32 s82, 0x3e38aa3b
	s_mov_b32 s88, 0xc01d265f
	s_mov_b32 s50, s69
	s_mov_b32 s86, s68
	s_mov_b32 s60, s49
	v_writelane_b32 v255, s87, 45
	s_branch .LBB0_314

.LBB0_561:
	s_and_b64 vcc, exec, s[16:17]
	s_cbranch_vccz .LBB0_711
	v_readlane_b32 s6, v254, 50
	v_readlane_b32 s7, v254, 46
	s_mul_i32 s6, s35, s6
	s_sub_i32 s7, s7, s36
	s_add_i32 s23, s7, s6
	s_lshl_b32 s22, s35, 3
	s_mov_b64 s[6:7], -1
	s_and_b64 vcc, exec, s[90:91]
	s_cbranch_vccz .LBB0_637
	v_mbcnt_lo_u32_b32 v66, -1, 0
	v_mbcnt_hi_u32_b32 v66, -1, v66
	s_getreg_b32 s6, hwreg(HW_REG_HW_ID, 0, 6)
	s_lshl_b32 s6, s6, 2
	s_and_b32 s6, s6, 0xfc
	s_or_b32 s6, s6, 0x27100
	v_mov_b32_e32 v0, s6
	ds_read_b32 v0, v0
	s_cmpk_gt_i32 s23, 0x211
	s_waitcnt lgkmcnt(0)
	v_readfirstlane_b32 s9, v0
	s_cbranch_scc1 .LBB0_636
	s_add_i32 s20, s23, 0xc05
	s_mul_hi_i32 s6, s20, 0x2aaaaaab
	s_lshr_b32 s7, s6, 31
	s_ashr_i32 s15, s6, 9
	s_add_i32 s15, s15, s7
	s_mul_i32 s16, s15, 0xfffff400
	s_add_i32 s16, s16, s20
	s_cmpk_gt_i32 s16, 0x7ff
	s_mov_b64 s[12:13], -1
	s_cbranch_scc0 .LBB0_566
	s_add_i32 s6, s16, 0xfffff800
	s_mov_b32 s10, 31
	s_lshl_b32 s7, s15, 5
	s_lshr_b32 s6, s6, 5
	s_lshl_b32 s24, s20, 8
	s_ashr_i32 s11, s10, 31
	s_add_i32 s6, s6, s7
	s_lshl_b32 s14, s20, 5
	s_and_b32 s8, s24, 0x300
	s_lshl_b64 s[10:11], s[10:11], 3
	s_add_u32 s10, s0, s10
	s_addc_u32 s11, s1, s11
	s_load_dwordx2 s[10:11], s[10:11], 0x0
	s_ashr_i32 s7, s6, 31
	s_lshl_b64 s[12:13], s[6:7], 20
	s_lshl_b64 s[6:7], s[6:7], 22
	s_waitcnt lgkmcnt(0)
	s_add_u32 s6, s10, s6
	s_mov_b32 s10, 35
	s_addc_u32 s7, s11, s7
	s_ashr_i32 s11, s10, 31
	s_lshl_b64 s[10:11], s[10:11], 3
	s_add_u32 s10, s0, s10
	s_addc_u32 s11, s1, s11
	s_load_dwordx2 s[10:11], s[10:11], 0x0
	s_waitcnt lgkmcnt(0)
	s_add_u32 s10, s10, s12
	s_addc_u32 s11, s11, s13
	s_add_u32 s10, s10, 0x12800000
	s_addc_u32 s11, s11, 0
	s_mov_b64 s[12:13], 0

.LBB0_569:
	v_lshl_or_b32 v67, s9, 6, v66
	v_ashrrev_i32_e32 v69, 6, v67
	s_and_b32 s14, s14, 0x380
	v_lshlrev_b32_e32 v135, 4, v69
	v_add_u32_e32 v0, s14, v135
	s_waitcnt vmcnt(0)
	v_mad_i64_i32 v[2:3], s[16:17], s12, v0, 0
	v_and_b32_e32 v68, 63, v66
	v_lshl_add_u64 v[2:3], v[2:3], 2, s[6:7]
	s_mov_b32 s9, s71
	v_lshl_add_u64 v[2:3], s[8:9], 2, v[2:3]
	v_lshlrev_b32_e32 v0, 4, v68
	v_lshl_add_u64 v[2:3], v[2:3], 0, v[0:1]
	s_lshl_b32 s70, s12, 2
	v_lshl_add_u64 v[10:11], v[2:3], 0, s[70:71]
	global_load_dwordx4 v[2:5], v[2:3], off nt
	s_nop 0
	global_load_dwordx4 v[6:9], v[10:11], off nt
	v_lshl_add_u64 v[10:11], v[10:11], 0, s[70:71]
	v_lshl_add_u64 v[18:19], v[10:11], 0, s[70:71]
	global_load_dwordx4 v[10:13], v[10:11], off nt
	s_nop 0
	global_load_dwordx4 v[14:17], v[18:19], off nt
	v_lshl_add_u64 v[18:19], v[18:19], 0, s[70:71]
	v_lshl_add_u64 v[26:27], v[18:19], 0, s[70:71]
	global_load_dwordx4 v[18:21], v[18:19], off nt
	s_nop 0
	global_load_dwordx4 v[22:25], v[26:27], off nt
	v_lshl_add_u64 v[26:27], v[26:27], 0, s[70:71]
	v_lshl_add_u64 v[34:35], v[26:27], 0, s[70:71]
	v_lshl_add_u64 v[38:39], v[34:35], 0, s[70:71]
	v_lshl_add_u64 v[42:43], v[38:39], 0, s[70:71]
	v_lshl_add_u64 v[46:47], v[42:43], 0, s[70:71]
	v_lshl_add_u64 v[50:51], v[46:47], 0, s[70:71]
	v_lshl_add_u64 v[54:55], v[50:51], 0, s[70:71]
	v_lshl_add_u64 v[58:59], v[54:55], 0, s[70:71]
	v_lshl_add_u64 v[62:63], v[58:59], 0, s[70:71]
	global_load_dwordx4 v[26:29], v[26:27], off nt
	s_nop 0
	global_load_dwordx4 v[30:33], v[34:35], off nt
	v_lshlrev_b32_e32 v134, 2, v68
	global_load_dwordx4 v[34:37], v[38:39], off nt
	v_lshl_add_u32 v0, v68, 9, 0
	global_load_dwordx4 v[38:41], v[42:43], off nt
	v_bitop3_b32 v68, v69, v66, 7 bitop3:0x78
	global_load_dwordx4 v[42:45], v[46:47], off nt
	v_lshrrev_b32_e32 v69, 5, v67
	global_load_dwordx4 v[46:49], v[50:51], off nt
	v_xor_b32_e32 v69, v69, v66
	global_load_dwordx4 v[50:53], v[54:55], off nt
	v_readlane_b32 s6, v254, 44
	global_load_dwordx4 v[54:57], v[58:59], off nt
	v_lshlrev_b32_e32 v69, 4, v69
	global_load_dwordx4 v[58:61], v[62:63], off nt
	v_lshl_add_u64 v[62:63], v[62:63], 0, s[70:71]
	global_load_dwordx4 v[62:65], v[62:63], off nt
	v_ashrrev_i32_e32 v140, 3, v67
	v_add_u32_e32 v70, 0x200, v67
	v_add_u32_e32 v71, 0x400, v67
	v_add_u32_e32 v67, 0x600, v67
	s_mul_i32 s26, s6, s35
	v_readlane_b32 s6, v254, 48
	v_and_b32_e32 v69, 0x70, v69
	v_lshlrev_b32_e32 v66, 4, v66
	v_ashrrev_i32_e32 v141, 3, v70
	v_ashrrev_i32_e32 v142, 3, v71
	v_ashrrev_i32_e32 v143, 3, v67
	s_mul_i32 s29, s6, s35
	v_readlane_b32 s6, v254, 51
	v_lshlrev_b32_e32 v68, 4, v68
	v_add_u32_e32 v69, 0, v69
	v_and_b32_e32 v136, 0x70, v66
	v_lshlrev_b32_e32 v66, 7, v140
	v_lshlrev_b32_e32 v70, 7, v141
	v_lshlrev_b32_e32 v71, 7, v142
	v_lshlrev_b32_e32 v67, 7, v143
	s_mul_i32 s6, s6, s35
	v_mov_b32_e32 v137, v1
	s_lshl_b32 s25, s35, 12
	s_lshl_b32 s27, s35, 4
	s_lshl_b32 s28, s35, 8
	s_add_i32 s30, s6, 0xbe5
	v_add_u32_e32 v144, v0, v68
	v_add_u32_e32 v145, v69, v66
	v_add_u32_e32 v146, v69, v70
	v_add_u32_e32 v147, v69, v71
	v_add_u32_e32 v148, v69, v67
	v_readlane_b32 s36, v254, 47
	s_mov_b32 s70, s14
	s_mov_b32 s37, s31
	s_mov_b32 s12, s8
	s_mov_b64 s[16:17], s[10:11]
	s_branch .LBB0_573

.LBB0_573:
	v_readlane_b32 s6, v254, 46
	s_add_i32 s6, s6, s29
	s_add_i32 s9, s20, s22
	s_add_i32 s7, s6, 0xbe5
	s_cmpk_lt_i32 s7, 0xe17
	s_cselect_b64 s[18:19], -1, 0
	s_cmpk_gt_i32 s7, 0xe16
	s_cbranch_scc1 .LBB0_580
	s_mul_hi_i32 s7, s7, 0x2aaaaaab
	s_lshr_b32 s12, s7, 31
	s_ashr_i32 s20, s7, 9
	s_add_i32 s20, s20, s12
	s_mul_i32 s7, s20, 0xfffff400
	s_add_i32 s37, s6, s7
	s_add_i32 s21, s37, 0xbe5
	s_cmpk_gt_i32 s21, 0x7ff
	s_mov_b64 s[14:15], -1
	s_cbranch_scc0 .LBB0_576
	s_addk_i32 s37, 0x3e5
	s_mov_b32 s14, 31
	s_lshl_b32 s6, s20, 5
	s_lshr_b32 s7, s37, 5
	s_ashr_i32 s15, s14, 31
	s_add_i32 s6, s7, s6
	s_lshl_b32 s13, s9, 5
	s_and_b32 s12, s24, 0x300
	s_lshl_b64 s[14:15], s[14:15], 3
	s_add_u32 s14, s0, s14
	s_addc_u32 s15, s1, s15
	s_load_dwordx2 s[14:15], s[14:15], 0x0
	s_ashr_i32 s7, s6, 31
	s_lshl_b64 s[16:17], s[6:7], 20
	s_lshl_b64 s[6:7], s[6:7], 22
	s_waitcnt lgkmcnt(0)
	s_add_u32 s6, s14, s6
	s_mov_b32 s14, 35
	s_addc_u32 s7, s15, s7
	s_ashr_i32 s15, s14, 31
	s_lshl_b64 s[14:15], s[14:15], 3
	s_add_u32 s14, s0, s14
	s_addc_u32 s15, s1, s15
	s_load_dwordx2 s[14:15], s[14:15], 0x0
	s_waitcnt lgkmcnt(0)
	s_add_u32 s14, s14, s16
	s_addc_u32 s15, s15, s17
	s_add_u32 s16, s14, 0x12800000
	s_addc_u32 s17, s15, 0
	s_mov_b64 s[14:15], 0

.LBB0_604:
	v_ashrrev_i32_e32 v139, 31, v138
	v_lshlrev_b64 v[138:139], 10, v[138:139]
	v_lshl_add_u64 v[138:139], s[10:11], 0, v[138:139]
	v_lshl_add_u64 v[138:139], v[138:139], 0, s[70:71]
	v_lshl_add_u64 v[138:139], v[138:139], 0, v[136:137]
	s_andn2_b64 vcc, exec, s[18:19]
	s_mov_b64 s[6:7], -1
	s_waitcnt lgkmcnt(0)
	global_store_dwordx4 v[138:139], v[130:133], off nt
	s_cbranch_vccnz .LBB0_572
	v_readlane_b32 s6, v254, 46
	s_add_i32 s6, s6, s26
	s_add_i32 s20, s9, s22
	s_add_i32 s7, s6, 0xbe5
	s_cmpk_gt_i32 s7, 0xe16
	s_cbranch_scc1 .LBB0_612
	s_mul_hi_i32 s7, s7, 0x2aaaaaab
	s_lshr_b32 s8, s7, 31
	s_ashr_i32 s13, s7, 9
	s_add_i32 s13, s13, s8
	s_mul_i32 s7, s13, 0xfffff400
	s_add_i32 s21, s6, s7
	s_add_i32 s15, s21, 0xbe5
	s_cmpk_gt_i32 s15, 0x7ff
	s_mov_b64 s[18:19], -1
	s_cbranch_scc0 .LBB0_608
	s_addk_i32 s21, 0x525
	s_mov_b32 s10, 31
	s_lshl_b32 s6, s13, 5
	s_lshr_b32 s7, s21, 5
	s_ashr_i32 s11, s10, 31
	s_add_i32 s6, s7, s6
	s_lshl_b32 s9, s20, 5
	s_and_b32 s8, s24, 0x300
	s_lshl_b64 s[10:11], s[10:11], 3
	s_add_u32 s10, s0, s10
	s_addc_u32 s11, s1, s11
	s_load_dwordx2 s[10:11], s[10:11], 0x0
	s_ashr_i32 s7, s6, 31
	s_lshl_b64 s[18:19], s[6:7], 20
	s_lshl_b64 s[6:7], s[6:7], 22
	s_waitcnt lgkmcnt(0)
	s_add_u32 s6, s10, s6
	s_mov_b32 s10, 35
	s_addc_u32 s7, s11, s7
	s_ashr_i32 s11, s10, 31
	s_lshl_b64 s[10:11], s[10:11], 3
	s_add_u32 s10, s0, s10
	s_addc_u32 s11, s1, s11
	s_load_dwordx2 s[10:11], s[10:11], 0x0
	s_waitcnt lgkmcnt(0)
	s_add_u32 s10, s10, s18
	s_addc_u32 s11, s11, s19
	s_add_u32 s10, s10, 0x12800000
	s_addc_u32 s11, s11, 0
	s_mov_b64 s[18:19], 0

.LBB0_1405:
	s_andn2_b64 vcc, exec, s[6:7]
	s_cbranch_vccnz .LBB0_1479
	v_mbcnt_lo_u32_b32 v66, -1, 0
	v_mbcnt_hi_u32_b32 v66, -1, v66
	s_getreg_b32 s6, hwreg(HW_REG_HW_ID, 0, 6)
	s_lshl_b32 s6, s6, 2
	s_and_b32 s6, s6, 0xfc
	s_or_b32 s6, s6, 0x27100
	v_mov_b32_e32 v0, s6
	ds_read_b32 v0, v0
	v_readlane_b32 s6, v254, 50
	v_readlane_b32 s7, v254, 46
	s_mul_i32 s6, s37, s6
	s_sub_i32 s7, s7, s40
	s_add_i32 s6, s7, s6
	s_cmpk_gt_i32 s6, 0x1df
	s_waitcnt lgkmcnt(0)
	v_readfirstlane_b32 s9, v0
	s_cbranch_scc1 .LBB0_1479
	s_add_i32 s20, s6, 0xa25
	s_mul_hi_i32 s6, s20, 0x2aaaaaab
	s_lshr_b32 s7, s6, 31
	s_ashr_i32 s15, s6, 9
	s_add_i32 s15, s15, s7
	s_mul_i32 s16, s15, 0xfffff400
	s_add_i32 s16, s16, s20
	s_cmpk_gt_i32 s16, 0x7ff
	s_mov_b64 s[12:13], -1
	s_cbranch_scc0 .LBB0_1409
	s_add_i32 s6, s16, 0xfffff800
	s_mov_b32 s10, 31
	s_lshl_b32 s7, s15, 5
	s_lshr_b32 s6, s6, 5
	s_lshl_b32 s22, s20, 8
	s_ashr_i32 s11, s10, 31
	s_add_i32 s6, s6, s7
	s_lshl_b32 s14, s20, 5
	s_and_b32 s8, s22, 0x300
	s_lshl_b64 s[10:11], s[10:11], 3
	s_add_u32 s10, s0, s10
	s_addc_u32 s11, s1, s11
	s_load_dwordx2 s[10:11], s[10:11], 0x0
	s_ashr_i32 s7, s6, 31
	s_lshl_b64 s[12:13], s[6:7], 20
	s_lshl_b64 s[6:7], s[6:7], 22
	s_waitcnt lgkmcnt(0)
	s_add_u32 s6, s10, s6
	s_mov_b32 s10, 35
	s_addc_u32 s7, s11, s7
	s_ashr_i32 s11, s10, 31
	s_lshl_b64 s[10:11], s[10:11], 3
	s_add_u32 s10, s0, s10
	s_addc_u32 s11, s1, s11
	s_load_dwordx2 s[10:11], s[10:11], 0x0
	s_waitcnt lgkmcnt(0)
	s_add_u32 s10, s10, s12
	s_addc_u32 s11, s11, s13
	s_add_u32 s10, s10, 0x12800000
	s_addc_u32 s11, s11, 0
	s_mov_b64 s[12:13], 0

.LBB0_1414:
	v_ashrrev_i32_e32 v139, 31, v138
	v_lshlrev_b64 v[138:139], 10, v[138:139]
	s_add_i32 s31, s31, s26
	v_readlane_b32 s6, v254, 46
	v_lshl_add_u64 v[138:139], s[16:17], 0, v[138:139]
	s_add_i32 s22, s22, s24
	s_add_i32 s25, s25, s26
	s_add_i32 s35, s35, s28
	s_add_i32 s29, s29, s26
	s_add_i32 s6, s6, s31
	v_lshl_add_u64 v[138:139], v[138:139], 0, s[14:15]
	s_cmpk_gt_i32 s6, 0xc04
	v_lshl_add_u64 v[138:139], v[138:139], 0, v[136:137]
	s_cselect_b64 s[6:7], -1, 0
	s_waitcnt lgkmcnt(0)
	global_store_dwordx4 v[138:139], v[130:133], off nt

.LBB0_1416:
	v_readlane_b32 s6, v254, 46
	s_add_i32 s6, s6, s29
	s_add_i32 s9, s20, s23
	s_add_i32 s7, s6, 0xa05
	s_cmpk_lt_i32 s7, 0xc05
	s_cselect_b64 s[18:19], -1, 0
	s_cmpk_gt_i32 s7, 0xc04
	s_cbranch_scc1 .LBB0_1423
	s_mul_hi_i32 s7, s7, 0x2aaaaaab
	s_lshr_b32 s12, s7, 31
	s_ashr_i32 s20, s7, 9
	s_add_i32 s20, s20, s12
	s_mul_i32 s7, s20, 0xfffff400
	s_add_i32 s37, s6, s7
	s_add_i32 s21, s37, 0xa05
	s_cmpk_gt_i32 s21, 0x7ff
	s_mov_b64 s[14:15], -1
	s_cbranch_scc0 .LBB0_1419
	s_addk_i32 s37, 0x205
	s_mov_b32 s14, 31
	s_lshl_b32 s6, s20, 5
	s_lshr_b32 s7, s37, 5
	s_ashr_i32 s15, s14, 31
	s_add_i32 s6, s7, s6
	s_lshl_b32 s13, s9, 5
	s_and_b32 s12, s22, 0x300
	s_lshl_b64 s[14:15], s[14:15], 3
	s_add_u32 s14, s0, s14
	s_addc_u32 s15, s1, s15
	s_load_dwordx2 s[14:15], s[14:15], 0x0
	s_ashr_i32 s7, s6, 31
	s_lshl_b64 s[16:17], s[6:7], 20
	s_lshl_b64 s[6:7], s[6:7], 22
	s_waitcnt lgkmcnt(0)
	s_add_u32 s6, s14, s6
	s_mov_b32 s14, 35
	s_addc_u32 s7, s15, s7
	s_ashr_i32 s15, s14, 31
	s_lshl_b64 s[14:15], s[14:15], 3
	s_add_u32 s14, s0, s14
	s_addc_u32 s15, s1, s15
	s_load_dwordx2 s[14:15], s[14:15], 0x0
	s_waitcnt lgkmcnt(0)
	s_add_u32 s14, s14, s16
	s_addc_u32 s15, s15, s17
	s_add_u32 s16, s14, 0x12800000
	s_addc_u32 s17, s15, 0
	s_mov_b64 s[14:15], 0

.LBB0_1447:
	v_ashrrev_i32_e32 v139, 31, v138
	v_lshlrev_b64 v[138:139], 10, v[138:139]
	v_lshl_add_u64 v[138:139], s[10:11], 0, v[138:139]
	v_lshl_add_u64 v[138:139], v[138:139], 0, s[70:71]
	v_lshl_add_u64 v[138:139], v[138:139], 0, v[136:137]
	s_andn2_b64 vcc, exec, s[18:19]
	s_mov_b64 s[6:7], -1
	s_waitcnt lgkmcnt(0)
	global_store_dwordx4 v[138:139], v[130:133], off nt
	s_cbranch_vccnz .LBB0_1415
	v_readlane_b32 s6, v254, 46
	s_add_i32 s6, s6, s25
	s_add_i32 s20, s9, s23
	s_add_i32 s7, s6, 0xa05
	s_cmpk_gt_i32 s7, 0xc04
	s_cbranch_scc1 .LBB0_1455
	s_mul_hi_i32 s7, s7, 0x2aaaaaab
	s_lshr_b32 s8, s7, 31
	s_ashr_i32 s13, s7, 9
	s_add_i32 s13, s13, s8
	s_mul_i32 s7, s13, 0xfffff400
	s_add_i32 s21, s6, s7
	s_add_i32 s15, s21, 0xa05
	s_cmpk_gt_i32 s15, 0x7ff
	s_mov_b64 s[18:19], -1
	s_cbranch_scc0 .LBB0_1451
	s_addk_i32 s21, 0x205
	s_mov_b32 s10, 31
	s_lshl_b32 s6, s13, 5
	s_lshr_b32 s7, s21, 5
	s_ashr_i32 s11, s10, 31
	s_add_i32 s6, s7, s6
	s_lshl_b32 s9, s20, 5
	s_and_b32 s8, s22, 0x300
	s_lshl_b64 s[10:11], s[10:11], 3
	s_add_u32 s10, s0, s10
	s_addc_u32 s11, s1, s11
	s_load_dwordx2 s[10:11], s[10:11], 0x0
	s_ashr_i32 s7, s6, 31
	s_lshl_b64 s[18:19], s[6:7], 20
	s_lshl_b64 s[6:7], s[6:7], 22
	s_waitcnt lgkmcnt(0)
	s_add_u32 s6, s10, s6
	s_mov_b32 s10, 35
	s_addc_u32 s7, s11, s7
	s_ashr_i32 s11, s10, 31
	s_lshl_b64 s[10:11], s[10:11], 3
	s_add_u32 s10, s0, s10
	s_addc_u32 s11, s1, s11
	s_load_dwordx2 s[10:11], s[10:11], 0x0
	s_waitcnt lgkmcnt(0)
	s_add_u32 s10, s10, s18
	s_addc_u32 s11, s11, s19
	s_add_u32 s10, s10, 0x12800000
	s_addc_u32 s11, s11, 0
	s_mov_b64 s[18:19], 0
